# mixer A cold-miss front-loading: at unit start the 512 threads touch every K/V row of the unit's key range (10 dword loads per thread) so the tile DMAs hit L2
# speedup vs baseline: 1.0100x; 1.0019x over previous
; __device__ __forceinline__ void mixer_a_phase(const bf16* AQ, const bf16* AK, const bf16* AV  , bf16* O, float* ST, float* ML, const float* rel_bias, LAS unsigned char* lds, int G, int blk, int tid, int lane, int wave) {
;     ...
;         const int i5 = lane & 31, hh = lane >> 5;
;         const size_t tb0 = (size_t)b * SEQ;
;         const bf16* Kb = AK + tb0 * 512 + h * 64; const bf16* Vb = AV + tb0 * 512 + h * 64;
;         bf16x8 qn[4];
;         { const bf16* qp = AQ + (tb0 + 512 * a + 32 * wave + i5) * 512 + h * 64 + 8 * hh;
; #pragma unroll
;           for (int d0 = 0; d0 < 4; ++d0) qn[d0] = *(const bf16x8*)(qp + 16 * d0); }
.LBB0_357:
	s_ashr_i32 s8, s43, 7
	s_bfe_u32 s1, s43, 0x40003
	s_ashr_i32 s9, s8, 31
	s_lshl_b32 s0, s1, 9
	s_lshl_b64 s[22:23], s[8:9], 13
	s_lshl_b32 s24, s44, 6
	s_lshl_b64 s[10:11], s[8:9], 23
	v_readlane_b32 s8, v255, 9
	v_readlane_b32 s9, v255, 10
	s_add_u32 s8, s8, s10
	s_addc_u32 s9, s9, s11
	s_or_b32 s26, s22, s0
	s_mov_b32 s27, s23
	v_lshl_add_u64 v[4:5], s[26:27], 0, v[138:139]
	v_readlane_b32 s34, v255, 7
	v_lshlrev_b64 v[4:5], 10, v[4:5]
	v_readlane_b32 s35, v255, 8
	s_lshl_b32 s16, s44, 7
	v_mov_b32_e32 v151, v3
	v_lshl_add_u64 v[4:5], s[34:35], 0, v[4:5]
	v_lshl_add_u64 v[4:5], v[4:5], 0, s[16:17]
	v_lshl_add_u64 v[4:5], v[4:5], 0, v[150:151]
	global_load_dwordx4 v[52:55], v[4:5], off
	global_load_dwordx4 v[56:59], v[4:5], off offset:32
	global_load_dwordx4 v[60:63], v[4:5], off offset:64
	global_load_dwordx4 v[64:67], v[4:5], off offset:96
	s_add_u32 s14, s86, s10
	s_addc_u32 s15, s87, s11
	s_add_u32 s28, s14, s16
	s_addc_u32 s29, s15, 0
	s_add_u32 s30, s8, s16
	v_cndmask_b32_e64 v2, 0, 1, s[18:19]
	s_mov_b32 s25, s17
	s_addc_u32 s31, s9, 0
	v_cmp_ne_u32_e64 s[8:9], 1, v2
	s_andn2_b64 vcc, exec, s[18:19]
	s_nop 0
	v_lshlrev_b32_e32 v68, 1, v142
	s_add_i32 s98, s0, 0xfffffc00
	v_add_u32_e32 v124, s98, v1
	v_mov_b32_e32 v125, v124
	v_max_i32_e32 v125, 0, v125
	v_min_i32_e32 v125, 0x1fff, v125
	v_lshlrev_b32_e32 v125, 10, v125
	global_load_dword v123, v125, s[28:29]
	global_load_dword v123, v125, s[30:31]
	v_add_u32_e32 v125, 0x200, v124
	v_max_i32_e32 v125, 0, v125
	v_min_i32_e32 v125, 0x1fff, v125
	v_lshlrev_b32_e32 v125, 10, v125
	global_load_dword v123, v125, s[28:29]
	global_load_dword v123, v125, s[30:31]
	v_add_u32_e32 v125, 0x400, v124
	v_max_i32_e32 v125, 0, v125
	v_min_i32_e32 v125, 0x1fff, v125
	v_lshlrev_b32_e32 v125, 10, v125
	global_load_dword v123, v125, s[28:29]
	global_load_dword v123, v125, s[30:31]
	v_add_u32_e32 v125, 0x600, v124
	v_max_i32_e32 v125, 0, v125
	v_min_i32_e32 v125, 0x1fff, v125
	v_lshlrev_b32_e32 v125, 10, v125
	global_load_dword v123, v125, s[28:29]
	global_load_dword v123, v125, s[30:31]
	v_add_u32_e32 v125, 0x800, v124
	v_max_i32_e32 v125, 0, v125
	v_min_i32_e32 v125, 0x1fff, v125
	v_lshlrev_b32_e32 v125, 10, v125
	global_load_dword v123, v125, s[28:29]
	global_load_dword v123, v125, s[30:31]
	s_cbranch_vccnz .LBB0_380
	v_mov_b32_e32 v5, s27
	v_or_b32_e32 v4, s26, v140
	v_lshlrev_b64 v[4:5], 10, v[4:5]
	v_mov_b32_e32 v69, v3
	v_add_u32_e32 v162, s0, v207
	v_lshl_add_u64 v[152:153], s[34:35], 0, v[4:5]
	v_lshl_add_u64 v[154:155], s[28:29], 0, v[68:69]
	v_lshl_add_u64 v[156:157], s[30:31], 0, v[68:69]
	v_readlane_b32 s14, v254, 59
